# adds P5 scan MFMA-slot LDS reads hoisted (p5_mfma) and P0 adaLN GEMV loads four batches deep (same FMA order), on top of pipelined quantizer draw and P4/P8 latency edits
# baseline (speedup 1.0000x reference)
; DI float sigmoidf_(float x) { return __builtin_amdgcn_rcpf(1.0f + __expf(-x)); }
; __global__ void __launch_bounds__(NWAVES * 64, 2) fwd_kernel(Args a_unused) {
;     ...
;             const int cb = item % 48, kq = item / 48, k0 = 512 * kq;
;             { const int k = k0 + tid; const float v = A->c[k], u = A->c_ctx[k]; sc[k] = v * sigmoidf_(v); scc[k] = u * sigmoidf_(u); }
;             __syncthreads();
;             const int col = 256 * cb + 4 * lane; const bool hasc = cb < 16;
;             f32x4 al = {0.f, 0.f, 0.f, 0.f}, ac = {0.f, 0.f, 0.f, 0.f};
; #pragma unroll 8
;             for (int k = k0 + wave; k < k0 + 512; k += 8) { const f32x4 wv = __builtin_nontemporal_load((const f32x4*)(A->w_mod + (size_t)k * 12288 + col)); al += sc[k] * wv; ac += scc[k] * wv; }
.LBB0_18:
	s_add_i32 s54, s12, 56
	s_mul_i32 s64, s12, 0xc000
	s_add_i32 s11, s12, -8
	s_mul_hi_i32 s55, s54, 0xc000
	s_add_i32 s54, s64, 0x2a0000
	v_subrev_u32_e32 v14, s13, v14
	v_ashrrev_i32_e32 v15, 31, v14
	s_waitcnt lgkmcnt(0)
	s_add_u32 s54, s8, s54
	v_lshlrev_b64 v[18:19], 2, v[14:15]
	s_addc_u32 s55, s9, s55
	v_lshl_add_u64 v[14:15], s[54:55], 0, v[18:19]
	s_add_i32 s13, s12, 8
	s_add_i32 s54, s64, 0x60000
	s_mul_hi_i32 s13, s13, 0xc000
	s_add_u32 s54, s8, s54
	v_ashrrev_i32_e32 v27, 31, v26
	s_addc_u32 s55, s9, s13
	v_lshl_add_u64 v[12:13], v[26:27], 2, s[8:9]
	s_mul_hi_i32 s13, s12, 0xc000
	s_add_u32 s8, s8, s64
	s_addc_u32 s9, s9, s13
	v_lshl_add_u64 v[16:17], s[54:55], 0, v[18:19]
	v_lshl_add_u64 v[18:19], s[8:9], 0, v[18:19]
	s_lshl_b32 s8, s12, 2
	s_add_i32 s8, s8, 0
	global_load_dwordx4 v[20:23], v[18:19], off nt
	global_load_dwordx4 v[46:49], v[16:17], off nt
	s_add_i32 s9, s11, 24
	s_add_i32 s54, s11, 32
	s_add_i32 s55, s11, 40
	s_add_i32 s64, s11, 48
	s_add_i32 s65, s11, 56
	v_mad_i64_i32 v[50:51], s[12:13], s9, v35, v[12:13]
	v_mad_i64_i32 v[54:55], s[12:13], s54, v35, v[12:13]
	v_mad_i64_i32 v[58:59], s[12:13], s55, v35, v[12:13]
	v_mad_i64_i32 v[62:63], s[12:13], s64, v35, v[12:13]
	v_mad_i64_i32 v[66:67], s[12:13], s65, v35, v[12:13]
	global_load_dwordx4 v[50:53], v[50:51], off nt
	s_nop 0
	global_load_dwordx4 v[54:57], v[54:55], off nt
	s_nop 0
	global_load_dwordx4 v[58:61], v[58:59], off nt
	s_nop 0
	global_load_dwordx4 v[62:65], v[62:63], off nt
	s_nop 0
	global_load_dwordx4 v[66:69], v[66:67], off nt
	s_nop 0
	global_load_dwordx4 v[70:73], v[14:15], off nt
	s_add_i32 s11, s11, 64
	v_lshl_add_u64 v[14:15], v[14:15], 0, s[60:61]
	v_lshl_add_u64 v[16:17], v[16:17], 0, s[60:61]
	v_lshl_add_u64 v[18:19], v[18:19], 0, s[60:61]
	global_load_dwordx4 v[104:107], v[18:19], off nt
	global_load_dwordx4 v[108:111], v[16:17], off nt
	s_add_i32 s9, s11, 24
	s_add_i32 s54, s11, 32
	s_add_i32 s55, s11, 40
	s_add_i32 s64, s11, 48
	s_add_i32 s65, s11, 56
	v_mad_i64_i32 v[112:113], s[12:13], s9, v35, v[12:13]
	v_mad_i64_i32 v[116:117], s[12:13], s54, v35, v[12:13]
	v_mad_i64_i32 v[120:121], s[12:13], s55, v35, v[12:13]
	v_mad_i64_i32 v[124:125], s[12:13], s64, v35, v[12:13]
	v_mad_i64_i32 v[128:129], s[12:13], s65, v35, v[12:13]
	global_load_dwordx4 v[112:115], v[112:113], off nt
	s_nop 0
	global_load_dwordx4 v[116:119], v[116:117], off nt
	s_nop 0
	global_load_dwordx4 v[120:123], v[120:121], off nt
	s_nop 0
	global_load_dwordx4 v[124:127], v[124:125], off nt
	s_nop 0
	global_load_dwordx4 v[128:131], v[128:129], off nt
	s_nop 0
	global_load_dwordx4 v[132:135], v[14:15], off nt
	s_add_i32 s11, s11, 64
	v_lshl_add_u64 v[14:15], v[14:15], 0, s[60:61]
	v_lshl_add_u64 v[16:17], v[16:17], 0, s[60:61]
	v_lshl_add_u64 v[18:19], v[18:19], 0, s[60:61]
	global_load_dwordx4 v[168:171], v[18:19], off nt
	global_load_dwordx4 v[172:175], v[16:17], off nt
	s_add_i32 s9, s11, 24
	s_add_i32 s54, s11, 32
	s_add_i32 s55, s11, 40
	s_add_i32 s64, s11, 48
	s_add_i32 s65, s11, 56
	v_mad_i64_i32 v[176:177], s[12:13], s9, v35, v[12:13]
	v_mad_i64_i32 v[180:181], s[12:13], s54, v35, v[12:13]
	v_mad_i64_i32 v[184:185], s[12:13], s55, v35, v[12:13]
	v_mad_i64_i32 v[188:189], s[12:13], s64, v35, v[12:13]
	v_mad_i64_i32 v[192:193], s[12:13], s65, v35, v[12:13]
	global_load_dwordx4 v[176:179], v[176:177], off nt
	s_nop 0
	global_load_dwordx4 v[180:183], v[180:181], off nt
	s_nop 0
	global_load_dwordx4 v[184:187], v[184:185], off nt
	s_nop 0
	global_load_dwordx4 v[188:191], v[188:189], off nt
	s_nop 0
	global_load_dwordx4 v[192:195], v[192:193], off nt
	s_nop 0
	global_load_dwordx4 v[196:199], v[14:15], off nt
	s_add_i32 s11, s11, 64
	v_lshl_add_u64 v[14:15], v[14:15], 0, s[60:61]
	v_lshl_add_u64 v[16:17], v[16:17], 0, s[60:61]
	v_lshl_add_u64 v[18:19], v[18:19], 0, s[60:61]
	global_load_dwordx4 v[200:203], v[18:19], off nt
	global_load_dwordx4 v[204:207], v[16:17], off nt
	s_add_i32 s9, s11, 24
	s_add_i32 s54, s11, 32
	s_add_i32 s55, s11, 40
	s_add_i32 s64, s11, 48
	s_add_i32 s65, s11, 56
	v_mad_i64_i32 v[208:209], s[12:13], s9, v35, v[12:13]
	v_mad_i64_i32 v[212:213], s[12:13], s54, v35, v[12:13]
	v_mad_i64_i32 v[216:217], s[12:13], s55, v35, v[12:13]
	v_mad_i64_i32 v[220:221], s[12:13], s64, v35, v[12:13]
	v_mad_i64_i32 v[224:225], s[12:13], s65, v35, v[12:13]
	global_load_dwordx4 v[208:211], v[208:209], off nt
	s_nop 0
	global_load_dwordx4 v[212:215], v[212:213], off nt
	s_nop 0
	global_load_dwordx4 v[216:219], v[216:217], off nt
	s_nop 0
	global_load_dwordx4 v[220:223], v[220:221], off nt
	s_nop 0
	global_load_dwordx4 v[224:227], v[224:225], off nt
	s_nop 0
	global_load_dwordx4 v[228:231], v[14:15], off nt
	s_add_i32 s11, s11, 64
	v_lshl_add_u64 v[14:15], v[14:15], 0, s[60:61]
	v_lshl_add_u64 v[16:17], v[16:17], 0, s[60:61]
	v_lshl_add_u64 v[18:19], v[18:19], 0, s[60:61]
	v_mov_b32_e32 v2, s8
	ds_read2_b32 v[28:29], v2 offset1:8
	v_add_u32_e32 v27, 0x2000, v2
	ds_read2_b32 v[74:75], v2 offset0:16 offset1:24
	ds_read2_b32 v[76:77], v2 offset0:32 offset1:40
	ds_read2_b32 v[78:79], v2 offset0:48 offset1:56
	ds_read2_b32 v[80:81], v27 offset1:8
	ds_read2_b32 v[82:83], v27 offset0:16 offset1:24
	ds_read2_b32 v[84:85], v27 offset0:32 offset1:40
	ds_read2_b32 v[86:87], v27 offset0:48 offset1:56
	s_waitcnt lgkmcnt(7)
	v_mov_b32_e32 v2, v29
	s_waitcnt lgkmcnt(3)
	v_mov_b32_e32 v94, v81
	v_mov_b32_e32 v88, v75
	s_waitcnt lgkmcnt(2)
	v_mov_b32_e32 v96, v83
	v_mov_b32_e32 v90, v77
	s_waitcnt lgkmcnt(1)
	v_mov_b32_e32 v98, v85
	s_addk_i32 s8, 0x100
	v_mov_b32_e32 v92, v79
	s_waitcnt lgkmcnt(0)
	v_mov_b32_e32 v100, v87
	s_waitcnt vmcnt(31)
; __global__ void __launch_bounds__(NWAVES * 64, 2) fwd_kernel(Args a_unused) {
;     ...
; #pragma unroll 8
;             for (int k = k0 + wave; k < k0 + 512; k += 8) { const f32x4 wv = __builtin_nontemporal_load((const f32x4*)(A->w_mod + (size_t)k * 12288 + col)); al += sc[k] * wv; ac += scc[k] * wv; }
	v_pk_fma_f32 v[6:7], v[22:23], v[28:29], v[6:7] op_sel_hi:[1,0,1]
	v_pk_fma_f32 v[4:5], v[20:21], v[28:29], v[4:5] op_sel_hi:[1,0,1]
	v_pk_fma_f32 v[10:11], v[22:23], v[80:81], v[10:11] op_sel_hi:[1,0,1]
	v_pk_fma_f32 v[8:9], v[20:21], v[80:81], v[8:9] op_sel_hi:[1,0,1]
	s_waitcnt vmcnt(30)
	v_pk_fma_f32 v[6:7], v[48:49], v[2:3], v[6:7] op_sel_hi:[1,0,1]
	v_pk_fma_f32 v[4:5], v[46:47], v[2:3], v[4:5] op_sel_hi:[1,0,1]
	v_pk_fma_f32 v[10:11], v[48:49], v[94:95], v[10:11] op_sel_hi:[1,0,1]
	v_pk_fma_f32 v[8:9], v[46:47], v[94:95], v[8:9] op_sel_hi:[1,0,1]
	s_waitcnt vmcnt(29)
	v_pk_fma_f32 v[6:7], v[52:53], v[74:75], v[6:7] op_sel_hi:[1,0,1]
	v_pk_fma_f32 v[4:5], v[50:51], v[74:75], v[4:5] op_sel_hi:[1,0,1]
	v_pk_fma_f32 v[10:11], v[52:53], v[82:83], v[10:11] op_sel_hi:[1,0,1]
	v_pk_fma_f32 v[8:9], v[50:51], v[82:83], v[8:9] op_sel_hi:[1,0,1]
	s_waitcnt vmcnt(28)
	v_pk_fma_f32 v[6:7], v[56:57], v[88:89], v[6:7] op_sel_hi:[1,0,1]
	v_pk_fma_f32 v[4:5], v[54:55], v[88:89], v[4:5] op_sel_hi:[1,0,1]
	v_pk_fma_f32 v[10:11], v[56:57], v[96:97], v[10:11] op_sel_hi:[1,0,1]
	v_pk_fma_f32 v[8:9], v[54:55], v[96:97], v[8:9] op_sel_hi:[1,0,1]
	s_waitcnt vmcnt(27)
	v_pk_fma_f32 v[6:7], v[60:61], v[76:77], v[6:7] op_sel_hi:[1,0,1]
	v_pk_fma_f32 v[4:5], v[58:59], v[76:77], v[4:5] op_sel_hi:[1,0,1]
	v_pk_fma_f32 v[10:11], v[60:61], v[84:85], v[10:11] op_sel_hi:[1,0,1]
	v_pk_fma_f32 v[8:9], v[58:59], v[84:85], v[8:9] op_sel_hi:[1,0,1]
	s_waitcnt vmcnt(26)
	v_pk_fma_f32 v[6:7], v[64:65], v[90:91], v[6:7] op_sel_hi:[1,0,1]
	v_pk_fma_f32 v[4:5], v[62:63], v[90:91], v[4:5] op_sel_hi:[1,0,1]
	v_pk_fma_f32 v[10:11], v[64:65], v[98:99], v[10:11] op_sel_hi:[1,0,1]
	v_pk_fma_f32 v[8:9], v[62:63], v[98:99], v[8:9] op_sel_hi:[1,0,1]
	s_waitcnt vmcnt(25)
	v_pk_fma_f32 v[6:7], v[68:69], v[78:79], v[6:7] op_sel_hi:[1,0,1]
	v_pk_fma_f32 v[4:5], v[66:67], v[78:79], v[4:5] op_sel_hi:[1,0,1]
	v_pk_fma_f32 v[10:11], v[68:69], v[86:87], v[10:11] op_sel_hi:[1,0,1]
	v_pk_fma_f32 v[8:9], v[66:67], v[86:87], v[8:9] op_sel_hi:[1,0,1]
	s_waitcnt vmcnt(24)
	v_pk_fma_f32 v[6:7], v[72:73], v[92:93], v[6:7] op_sel_hi:[1,0,1]
	v_pk_fma_f32 v[4:5], v[70:71], v[92:93], v[4:5] op_sel_hi:[1,0,1]
	v_pk_fma_f32 v[10:11], v[72:73], v[100:101], v[10:11] op_sel_hi:[1,0,1]
	v_pk_fma_f32 v[8:9], v[70:71], v[100:101], v[8:9] op_sel_hi:[1,0,1]
	global_load_dwordx4 v[20:23], v[18:19], off nt
	global_load_dwordx4 v[46:49], v[16:17], off nt
	s_add_i32 s9, s11, 24
	s_add_i32 s54, s11, 32
	s_add_i32 s55, s11, 40
	s_add_i32 s64, s11, 48
	s_add_i32 s65, s11, 56
	v_mad_i64_i32 v[50:51], s[12:13], s9, v35, v[12:13]
	v_mad_i64_i32 v[54:55], s[12:13], s54, v35, v[12:13]
	v_mad_i64_i32 v[58:59], s[12:13], s55, v35, v[12:13]
	v_mad_i64_i32 v[62:63], s[12:13], s64, v35, v[12:13]
	v_mad_i64_i32 v[66:67], s[12:13], s65, v35, v[12:13]
	global_load_dwordx4 v[50:53], v[50:51], off nt
	s_nop 0
	global_load_dwordx4 v[54:57], v[54:55], off nt
	s_nop 0
	global_load_dwordx4 v[58:61], v[58:59], off nt
	s_nop 0
	global_load_dwordx4 v[62:65], v[62:63], off nt
	s_nop 0
	global_load_dwordx4 v[66:69], v[66:67], off nt
	s_nop 0
	global_load_dwordx4 v[70:73], v[14:15], off nt
	s_add_i32 s11, s11, 64
	v_lshl_add_u64 v[14:15], v[14:15], 0, s[60:61]
	v_lshl_add_u64 v[16:17], v[16:17], 0, s[60:61]
	v_lshl_add_u64 v[18:19], v[18:19], 0, s[60:61]
	v_mov_b32_e32 v2, s8
	ds_read2_b32 v[28:29], v2 offset1:8
	v_add_u32_e32 v27, 0x2000, v2
	ds_read2_b32 v[74:75], v2 offset0:16 offset1:24
	ds_read2_b32 v[76:77], v2 offset0:32 offset1:40
	ds_read2_b32 v[78:79], v2 offset0:48 offset1:56
	ds_read2_b32 v[80:81], v27 offset1:8
	ds_read2_b32 v[82:83], v27 offset0:16 offset1:24
	ds_read2_b32 v[84:85], v27 offset0:32 offset1:40
	ds_read2_b32 v[86:87], v27 offset0:48 offset1:56
	s_waitcnt lgkmcnt(7)
	v_mov_b32_e32 v2, v29
	s_waitcnt lgkmcnt(3)
	v_mov_b32_e32 v94, v81
	v_mov_b32_e32 v88, v75
	s_waitcnt lgkmcnt(2)
	v_mov_b32_e32 v96, v83
	v_mov_b32_e32 v90, v77
	s_waitcnt lgkmcnt(1)
	v_mov_b32_e32 v98, v85
	s_addk_i32 s8, 0x100
	v_mov_b32_e32 v92, v79
	s_waitcnt lgkmcnt(0)
	v_mov_b32_e32 v100, v87
	s_waitcnt vmcnt(31)
	v_pk_fma_f32 v[6:7], v[106:107], v[28:29], v[6:7] op_sel_hi:[1,0,1]
	v_pk_fma_f32 v[4:5], v[104:105], v[28:29], v[4:5] op_sel_hi:[1,0,1]
	v_pk_fma_f32 v[10:11], v[106:107], v[80:81], v[10:11] op_sel_hi:[1,0,1]
	v_pk_fma_f32 v[8:9], v[104:105], v[80:81], v[8:9] op_sel_hi:[1,0,1]
	s_waitcnt vmcnt(30)
	v_pk_fma_f32 v[6:7], v[110:111], v[2:3], v[6:7] op_sel_hi:[1,0,1]
	v_pk_fma_f32 v[4:5], v[108:109], v[2:3], v[4:5] op_sel_hi:[1,0,1]
	v_pk_fma_f32 v[10:11], v[110:111], v[94:95], v[10:11] op_sel_hi:[1,0,1]
	v_pk_fma_f32 v[8:9], v[108:109], v[94:95], v[8:9] op_sel_hi:[1,0,1]
	s_waitcnt vmcnt(29)
	v_pk_fma_f32 v[6:7], v[114:115], v[74:75], v[6:7] op_sel_hi:[1,0,1]
	v_pk_fma_f32 v[4:5], v[112:113], v[74:75], v[4:5] op_sel_hi:[1,0,1]
	v_pk_fma_f32 v[10:11], v[114:115], v[82:83], v[10:11] op_sel_hi:[1,0,1]
	v_pk_fma_f32 v[8:9], v[112:113], v[82:83], v[8:9] op_sel_hi:[1,0,1]
	s_waitcnt vmcnt(28)
	v_pk_fma_f32 v[6:7], v[118:119], v[88:89], v[6:7] op_sel_hi:[1,0,1]
	v_pk_fma_f32 v[4:5], v[116:117], v[88:89], v[4:5] op_sel_hi:[1,0,1]
	v_pk_fma_f32 v[10:11], v[118:119], v[96:97], v[10:11] op_sel_hi:[1,0,1]
	v_pk_fma_f32 v[8:9], v[116:117], v[96:97], v[8:9] op_sel_hi:[1,0,1]
	s_waitcnt vmcnt(27)
	v_pk_fma_f32 v[6:7], v[122:123], v[76:77], v[6:7] op_sel_hi:[1,0,1]
	v_pk_fma_f32 v[4:5], v[120:121], v[76:77], v[4:5] op_sel_hi:[1,0,1]
	v_pk_fma_f32 v[10:11], v[122:123], v[84:85], v[10:11] op_sel_hi:[1,0,1]
	v_pk_fma_f32 v[8:9], v[120:121], v[84:85], v[8:9] op_sel_hi:[1,0,1]
	s_waitcnt vmcnt(26)
; __global__ void __launch_bounds__(NWAVES * 64, 2) fwd_kernel(Args a_unused) {
;     ...
; #pragma unroll 8
;             for (int k = k0 + wave; k < k0 + 512; k += 8) { const f32x4 wv = __builtin_nontemporal_load((const f32x4*)(A->w_mod + (size_t)k * 12288 + col)); al += sc[k] * wv; ac += scc[k] * wv; }
	v_pk_fma_f32 v[6:7], v[126:127], v[90:91], v[6:7] op_sel_hi:[1,0,1]
	v_pk_fma_f32 v[4:5], v[124:125], v[90:91], v[4:5] op_sel_hi:[1,0,1]
	v_pk_fma_f32 v[10:11], v[126:127], v[98:99], v[10:11] op_sel_hi:[1,0,1]
	v_pk_fma_f32 v[8:9], v[124:125], v[98:99], v[8:9] op_sel_hi:[1,0,1]
	s_waitcnt vmcnt(25)
	v_pk_fma_f32 v[6:7], v[130:131], v[78:79], v[6:7] op_sel_hi:[1,0,1]
	v_pk_fma_f32 v[4:5], v[128:129], v[78:79], v[4:5] op_sel_hi:[1,0,1]
	v_pk_fma_f32 v[10:11], v[130:131], v[86:87], v[10:11] op_sel_hi:[1,0,1]
	v_pk_fma_f32 v[8:9], v[128:129], v[86:87], v[8:9] op_sel_hi:[1,0,1]
	s_waitcnt vmcnt(24)
	v_pk_fma_f32 v[6:7], v[134:135], v[92:93], v[6:7] op_sel_hi:[1,0,1]
	v_pk_fma_f32 v[4:5], v[132:133], v[92:93], v[4:5] op_sel_hi:[1,0,1]
	v_pk_fma_f32 v[10:11], v[134:135], v[100:101], v[10:11] op_sel_hi:[1,0,1]
	v_pk_fma_f32 v[8:9], v[132:133], v[100:101], v[8:9] op_sel_hi:[1,0,1]
	global_load_dwordx4 v[104:107], v[18:19], off nt
	global_load_dwordx4 v[108:111], v[16:17], off nt
	s_add_i32 s9, s11, 24
	s_add_i32 s54, s11, 32
	s_add_i32 s55, s11, 40
	s_add_i32 s64, s11, 48
	s_add_i32 s65, s11, 56
	v_mad_i64_i32 v[112:113], s[12:13], s9, v35, v[12:13]
	v_mad_i64_i32 v[116:117], s[12:13], s54, v35, v[12:13]
	v_mad_i64_i32 v[120:121], s[12:13], s55, v35, v[12:13]
	v_mad_i64_i32 v[124:125], s[12:13], s64, v35, v[12:13]
	v_mad_i64_i32 v[128:129], s[12:13], s65, v35, v[12:13]
	global_load_dwordx4 v[112:115], v[112:113], off nt
	s_nop 0
	global_load_dwordx4 v[116:119], v[116:117], off nt
	s_nop 0
	global_load_dwordx4 v[120:123], v[120:121], off nt
	s_nop 0
	global_load_dwordx4 v[124:127], v[124:125], off nt
	s_nop 0
	global_load_dwordx4 v[128:131], v[128:129], off nt
	s_nop 0
	global_load_dwordx4 v[132:135], v[14:15], off nt
	s_add_i32 s11, s11, 64
	v_lshl_add_u64 v[14:15], v[14:15], 0, s[60:61]
	v_lshl_add_u64 v[16:17], v[16:17], 0, s[60:61]
	v_lshl_add_u64 v[18:19], v[18:19], 0, s[60:61]
	v_mov_b32_e32 v2, s8
	ds_read2_b32 v[28:29], v2 offset1:8
	v_add_u32_e32 v27, 0x2000, v2
	ds_read2_b32 v[74:75], v2 offset0:16 offset1:24
	ds_read2_b32 v[76:77], v2 offset0:32 offset1:40
	ds_read2_b32 v[78:79], v2 offset0:48 offset1:56
	ds_read2_b32 v[80:81], v27 offset1:8
	ds_read2_b32 v[82:83], v27 offset0:16 offset1:24
	ds_read2_b32 v[84:85], v27 offset0:32 offset1:40
	ds_read2_b32 v[86:87], v27 offset0:48 offset1:56
	s_waitcnt lgkmcnt(7)
	v_mov_b32_e32 v2, v29
	s_waitcnt lgkmcnt(3)
	v_mov_b32_e32 v94, v81
	v_mov_b32_e32 v88, v75
	s_waitcnt lgkmcnt(2)
	v_mov_b32_e32 v96, v83
	v_mov_b32_e32 v90, v77
	s_waitcnt lgkmcnt(1)
	v_mov_b32_e32 v98, v85
	s_addk_i32 s8, 0x100
	v_mov_b32_e32 v92, v79
	s_waitcnt lgkmcnt(0)
	v_mov_b32_e32 v100, v87
	s_waitcnt vmcnt(31)
	v_pk_fma_f32 v[6:7], v[170:171], v[28:29], v[6:7] op_sel_hi:[1,0,1]
	v_pk_fma_f32 v[4:5], v[168:169], v[28:29], v[4:5] op_sel_hi:[1,0,1]
	v_pk_fma_f32 v[10:11], v[170:171], v[80:81], v[10:11] op_sel_hi:[1,0,1]
	v_pk_fma_f32 v[8:9], v[168:169], v[80:81], v[8:9] op_sel_hi:[1,0,1]
	s_waitcnt vmcnt(30)
	v_pk_fma_f32 v[6:7], v[174:175], v[2:3], v[6:7] op_sel_hi:[1,0,1]
	v_pk_fma_f32 v[4:5], v[172:173], v[2:3], v[4:5] op_sel_hi:[1,0,1]
	v_pk_fma_f32 v[10:11], v[174:175], v[94:95], v[10:11] op_sel_hi:[1,0,1]
	v_pk_fma_f32 v[8:9], v[172:173], v[94:95], v[8:9] op_sel_hi:[1,0,1]
	s_waitcnt vmcnt(29)
	v_pk_fma_f32 v[6:7], v[178:179], v[74:75], v[6:7] op_sel_hi:[1,0,1]
	v_pk_fma_f32 v[4:5], v[176:177], v[74:75], v[4:5] op_sel_hi:[1,0,1]
	v_pk_fma_f32 v[10:11], v[178:179], v[82:83], v[10:11] op_sel_hi:[1,0,1]
	v_pk_fma_f32 v[8:9], v[176:177], v[82:83], v[8:9] op_sel_hi:[1,0,1]
	s_waitcnt vmcnt(28)
	v_pk_fma_f32 v[6:7], v[182:183], v[88:89], v[6:7] op_sel_hi:[1,0,1]
	v_pk_fma_f32 v[4:5], v[180:181], v[88:89], v[4:5] op_sel_hi:[1,0,1]
	v_pk_fma_f32 v[10:11], v[182:183], v[96:97], v[10:11] op_sel_hi:[1,0,1]
	v_pk_fma_f32 v[8:9], v[180:181], v[96:97], v[8:9] op_sel_hi:[1,0,1]
	s_waitcnt vmcnt(27)
	v_pk_fma_f32 v[6:7], v[186:187], v[76:77], v[6:7] op_sel_hi:[1,0,1]
	v_pk_fma_f32 v[4:5], v[184:185], v[76:77], v[4:5] op_sel_hi:[1,0,1]
	v_pk_fma_f32 v[10:11], v[186:187], v[84:85], v[10:11] op_sel_hi:[1,0,1]
	v_pk_fma_f32 v[8:9], v[184:185], v[84:85], v[8:9] op_sel_hi:[1,0,1]
	s_waitcnt vmcnt(26)
	v_pk_fma_f32 v[6:7], v[190:191], v[90:91], v[6:7] op_sel_hi:[1,0,1]
	v_pk_fma_f32 v[4:5], v[188:189], v[90:91], v[4:5] op_sel_hi:[1,0,1]
	v_pk_fma_f32 v[10:11], v[190:191], v[98:99], v[10:11] op_sel_hi:[1,0,1]
	v_pk_fma_f32 v[8:9], v[188:189], v[98:99], v[8:9] op_sel_hi:[1,0,1]
	s_waitcnt vmcnt(25)
	v_pk_fma_f32 v[6:7], v[194:195], v[78:79], v[6:7] op_sel_hi:[1,0,1]
	v_pk_fma_f32 v[4:5], v[192:193], v[78:79], v[4:5] op_sel_hi:[1,0,1]
	v_pk_fma_f32 v[10:11], v[194:195], v[86:87], v[10:11] op_sel_hi:[1,0,1]
	v_pk_fma_f32 v[8:9], v[192:193], v[86:87], v[8:9] op_sel_hi:[1,0,1]
	s_waitcnt vmcnt(24)
; __global__ void __launch_bounds__(NWAVES * 64, 2) fwd_kernel(Args a_unused) {
;     ...
; #pragma unroll 8
;             for (int k = k0 + wave; k < k0 + 512; k += 8) { const f32x4 wv = __builtin_nontemporal_load((const f32x4*)(A->w_mod + (size_t)k * 12288 + col)); al += sc[k] * wv; ac += scc[k] * wv; }
	v_pk_fma_f32 v[6:7], v[198:199], v[92:93], v[6:7] op_sel_hi:[1,0,1]
	v_pk_fma_f32 v[4:5], v[196:197], v[92:93], v[4:5] op_sel_hi:[1,0,1]
	v_pk_fma_f32 v[10:11], v[198:199], v[100:101], v[10:11] op_sel_hi:[1,0,1]
	v_pk_fma_f32 v[8:9], v[196:197], v[100:101], v[8:9] op_sel_hi:[1,0,1]
	global_load_dwordx4 v[168:171], v[18:19], off nt
	global_load_dwordx4 v[172:175], v[16:17], off nt
	s_add_i32 s9, s11, 24
	s_add_i32 s54, s11, 32
	s_add_i32 s55, s11, 40
	s_add_i32 s64, s11, 48
	s_add_i32 s65, s11, 56
	v_mad_i64_i32 v[176:177], s[12:13], s9, v35, v[12:13]
	v_mad_i64_i32 v[180:181], s[12:13], s54, v35, v[12:13]
	v_mad_i64_i32 v[184:185], s[12:13], s55, v35, v[12:13]
	v_mad_i64_i32 v[188:189], s[12:13], s64, v35, v[12:13]
	v_mad_i64_i32 v[192:193], s[12:13], s65, v35, v[12:13]
	global_load_dwordx4 v[176:179], v[176:177], off nt
	s_nop 0
	global_load_dwordx4 v[180:183], v[180:181], off nt
	s_nop 0
	global_load_dwordx4 v[184:187], v[184:185], off nt
	s_nop 0
	global_load_dwordx4 v[188:191], v[188:189], off nt
	s_nop 0
	global_load_dwordx4 v[192:195], v[192:193], off nt
	s_nop 0
	global_load_dwordx4 v[196:199], v[14:15], off nt
	s_add_i32 s11, s11, 64
	v_lshl_add_u64 v[14:15], v[14:15], 0, s[60:61]
	v_lshl_add_u64 v[16:17], v[16:17], 0, s[60:61]
	v_lshl_add_u64 v[18:19], v[18:19], 0, s[60:61]
	v_mov_b32_e32 v2, s8
	ds_read2_b32 v[28:29], v2 offset1:8
	v_add_u32_e32 v27, 0x2000, v2
	ds_read2_b32 v[74:75], v2 offset0:16 offset1:24
	ds_read2_b32 v[76:77], v2 offset0:32 offset1:40
	ds_read2_b32 v[78:79], v2 offset0:48 offset1:56
	ds_read2_b32 v[80:81], v27 offset1:8
	ds_read2_b32 v[82:83], v27 offset0:16 offset1:24
	ds_read2_b32 v[84:85], v27 offset0:32 offset1:40
	ds_read2_b32 v[86:87], v27 offset0:48 offset1:56
	s_waitcnt lgkmcnt(7)
	v_mov_b32_e32 v2, v29
	s_waitcnt lgkmcnt(3)
	v_mov_b32_e32 v94, v81
	v_mov_b32_e32 v88, v75
	s_waitcnt lgkmcnt(2)
	v_mov_b32_e32 v96, v83
	v_mov_b32_e32 v90, v77
	s_waitcnt lgkmcnt(1)
	v_mov_b32_e32 v98, v85
	s_addk_i32 s8, 0x100
	v_mov_b32_e32 v92, v79
	s_waitcnt lgkmcnt(0)
	v_mov_b32_e32 v100, v87
	s_waitcnt vmcnt(31)
	v_pk_fma_f32 v[6:7], v[202:203], v[28:29], v[6:7] op_sel_hi:[1,0,1]
	v_pk_fma_f32 v[4:5], v[200:201], v[28:29], v[4:5] op_sel_hi:[1,0,1]
	v_pk_fma_f32 v[10:11], v[202:203], v[80:81], v[10:11] op_sel_hi:[1,0,1]
	v_pk_fma_f32 v[8:9], v[200:201], v[80:81], v[8:9] op_sel_hi:[1,0,1]
	s_waitcnt vmcnt(30)
	v_pk_fma_f32 v[6:7], v[206:207], v[2:3], v[6:7] op_sel_hi:[1,0,1]
	v_pk_fma_f32 v[4:5], v[204:205], v[2:3], v[4:5] op_sel_hi:[1,0,1]
	v_pk_fma_f32 v[10:11], v[206:207], v[94:95], v[10:11] op_sel_hi:[1,0,1]
	v_pk_fma_f32 v[8:9], v[204:205], v[94:95], v[8:9] op_sel_hi:[1,0,1]
	s_waitcnt vmcnt(29)
	v_pk_fma_f32 v[6:7], v[210:211], v[74:75], v[6:7] op_sel_hi:[1,0,1]
	v_pk_fma_f32 v[4:5], v[208:209], v[74:75], v[4:5] op_sel_hi:[1,0,1]
	v_pk_fma_f32 v[10:11], v[210:211], v[82:83], v[10:11] op_sel_hi:[1,0,1]
	v_pk_fma_f32 v[8:9], v[208:209], v[82:83], v[8:9] op_sel_hi:[1,0,1]
	s_waitcnt vmcnt(28)
	v_pk_fma_f32 v[6:7], v[214:215], v[88:89], v[6:7] op_sel_hi:[1,0,1]
	v_pk_fma_f32 v[4:5], v[212:213], v[88:89], v[4:5] op_sel_hi:[1,0,1]
	v_pk_fma_f32 v[10:11], v[214:215], v[96:97], v[10:11] op_sel_hi:[1,0,1]
	v_pk_fma_f32 v[8:9], v[212:213], v[96:97], v[8:9] op_sel_hi:[1,0,1]
	s_waitcnt vmcnt(27)
	v_pk_fma_f32 v[6:7], v[218:219], v[76:77], v[6:7] op_sel_hi:[1,0,1]
	v_pk_fma_f32 v[4:5], v[216:217], v[76:77], v[4:5] op_sel_hi:[1,0,1]
	v_pk_fma_f32 v[10:11], v[218:219], v[84:85], v[10:11] op_sel_hi:[1,0,1]
	v_pk_fma_f32 v[8:9], v[216:217], v[84:85], v[8:9] op_sel_hi:[1,0,1]
	s_waitcnt vmcnt(26)
	v_pk_fma_f32 v[6:7], v[222:223], v[90:91], v[6:7] op_sel_hi:[1,0,1]
	v_pk_fma_f32 v[4:5], v[220:221], v[90:91], v[4:5] op_sel_hi:[1,0,1]
	v_pk_fma_f32 v[10:11], v[222:223], v[98:99], v[10:11] op_sel_hi:[1,0,1]
	v_pk_fma_f32 v[8:9], v[220:221], v[98:99], v[8:9] op_sel_hi:[1,0,1]
	s_waitcnt vmcnt(25)
	v_pk_fma_f32 v[6:7], v[226:227], v[78:79], v[6:7] op_sel_hi:[1,0,1]
	v_pk_fma_f32 v[4:5], v[224:225], v[78:79], v[4:5] op_sel_hi:[1,0,1]
	v_pk_fma_f32 v[10:11], v[226:227], v[86:87], v[10:11] op_sel_hi:[1,0,1]
	v_pk_fma_f32 v[8:9], v[224:225], v[86:87], v[8:9] op_sel_hi:[1,0,1]
	s_waitcnt vmcnt(24)
	v_pk_fma_f32 v[6:7], v[230:231], v[92:93], v[6:7] op_sel_hi:[1,0,1]
	v_pk_fma_f32 v[4:5], v[228:229], v[92:93], v[4:5] op_sel_hi:[1,0,1]
	v_pk_fma_f32 v[10:11], v[230:231], v[100:101], v[10:11] op_sel_hi:[1,0,1]
	v_pk_fma_f32 v[8:9], v[228:229], v[100:101], v[8:9] op_sel_hi:[1,0,1]
	global_load_dwordx4 v[200:203], v[18:19], off nt
	global_load_dwordx4 v[204:207], v[16:17], off nt
	s_add_i32 s9, s11, 24
	s_add_i32 s54, s11, 32
	s_add_i32 s55, s11, 40
	s_add_i32 s64, s11, 48
	s_add_i32 s65, s11, 56
	v_mad_i64_i32 v[208:209], s[12:13], s9, v35, v[12:13]
	v_mad_i64_i32 v[212:213], s[12:13], s54, v35, v[12:13]
	v_mad_i64_i32 v[216:217], s[12:13], s55, v35, v[12:13]
	v_mad_i64_i32 v[220:221], s[12:13], s64, v35, v[12:13]
	v_mad_i64_i32 v[224:225], s[12:13], s65, v35, v[12:13]
	global_load_dwordx4 v[208:211], v[208:209], off nt
	s_nop 0
	global_load_dwordx4 v[212:215], v[212:213], off nt
	s_nop 0
	global_load_dwordx4 v[216:219], v[216:217], off nt
	s_nop 0
	global_load_dwordx4 v[220:223], v[220:221], off nt
	s_nop 0
	global_load_dwordx4 v[224:227], v[224:225], off nt
	s_nop 0
	global_load_dwordx4 v[228:231], v[14:15], off nt
	s_add_i32 s11, s11, 64
	v_lshl_add_u64 v[14:15], v[14:15], 0, s[60:61]
	v_lshl_add_u64 v[16:17], v[16:17], 0, s[60:61]
	v_lshl_add_u64 v[18:19], v[18:19], 0, s[60:61]
	v_mov_b32_e32 v2, s8
	ds_read2_b32 v[28:29], v2 offset1:8
	v_add_u32_e32 v27, 0x2000, v2
	ds_read2_b32 v[74:75], v2 offset0:16 offset1:24
	ds_read2_b32 v[76:77], v2 offset0:32 offset1:40
	ds_read2_b32 v[78:79], v2 offset0:48 offset1:56
	ds_read2_b32 v[80:81], v27 offset1:8
	ds_read2_b32 v[82:83], v27 offset0:16 offset1:24
	ds_read2_b32 v[84:85], v27 offset0:32 offset1:40
	ds_read2_b32 v[86:87], v27 offset0:48 offset1:56
	s_waitcnt lgkmcnt(7)
; __global__ void __launch_bounds__(NWAVES * 64, 2) fwd_kernel(Args a_unused) {
;     ...
; #pragma unroll 8
;             for (int k = k0 + wave; k < k0 + 512; k += 8) { const f32x4 wv = __builtin_nontemporal_load((const f32x4*)(A->w_mod + (size_t)k * 12288 + col)); al += sc[k] * wv; ac += scc[k] * wv; }
	v_mov_b32_e32 v2, v29
	s_waitcnt lgkmcnt(3)
	v_mov_b32_e32 v94, v81
	v_mov_b32_e32 v88, v75
	s_waitcnt lgkmcnt(2)
	v_mov_b32_e32 v96, v83
	v_mov_b32_e32 v90, v77
	s_waitcnt lgkmcnt(1)
	v_mov_b32_e32 v98, v85
	s_addk_i32 s8, 0x100
	v_mov_b32_e32 v92, v79
	s_waitcnt lgkmcnt(0)
	v_mov_b32_e32 v100, v87
	s_waitcnt vmcnt(31)
	v_pk_fma_f32 v[6:7], v[22:23], v[28:29], v[6:7] op_sel_hi:[1,0,1]
	v_pk_fma_f32 v[4:5], v[20:21], v[28:29], v[4:5] op_sel_hi:[1,0,1]
	v_pk_fma_f32 v[10:11], v[22:23], v[80:81], v[10:11] op_sel_hi:[1,0,1]
	v_pk_fma_f32 v[8:9], v[20:21], v[80:81], v[8:9] op_sel_hi:[1,0,1]
	s_waitcnt vmcnt(30)
	v_pk_fma_f32 v[6:7], v[48:49], v[2:3], v[6:7] op_sel_hi:[1,0,1]
	v_pk_fma_f32 v[4:5], v[46:47], v[2:3], v[4:5] op_sel_hi:[1,0,1]
	v_pk_fma_f32 v[10:11], v[48:49], v[94:95], v[10:11] op_sel_hi:[1,0,1]
	v_pk_fma_f32 v[8:9], v[46:47], v[94:95], v[8:9] op_sel_hi:[1,0,1]
	s_waitcnt vmcnt(29)
	v_pk_fma_f32 v[6:7], v[52:53], v[74:75], v[6:7] op_sel_hi:[1,0,1]
	v_pk_fma_f32 v[4:5], v[50:51], v[74:75], v[4:5] op_sel_hi:[1,0,1]
	v_pk_fma_f32 v[10:11], v[52:53], v[82:83], v[10:11] op_sel_hi:[1,0,1]
	v_pk_fma_f32 v[8:9], v[50:51], v[82:83], v[8:9] op_sel_hi:[1,0,1]
	s_waitcnt vmcnt(28)
	v_pk_fma_f32 v[6:7], v[56:57], v[88:89], v[6:7] op_sel_hi:[1,0,1]
	v_pk_fma_f32 v[4:5], v[54:55], v[88:89], v[4:5] op_sel_hi:[1,0,1]
	v_pk_fma_f32 v[10:11], v[56:57], v[96:97], v[10:11] op_sel_hi:[1,0,1]
	v_pk_fma_f32 v[8:9], v[54:55], v[96:97], v[8:9] op_sel_hi:[1,0,1]
	s_waitcnt vmcnt(27)
	v_pk_fma_f32 v[6:7], v[60:61], v[76:77], v[6:7] op_sel_hi:[1,0,1]
	v_pk_fma_f32 v[4:5], v[58:59], v[76:77], v[4:5] op_sel_hi:[1,0,1]
	v_pk_fma_f32 v[10:11], v[60:61], v[84:85], v[10:11] op_sel_hi:[1,0,1]
	v_pk_fma_f32 v[8:9], v[58:59], v[84:85], v[8:9] op_sel_hi:[1,0,1]
	s_waitcnt vmcnt(26)
	v_pk_fma_f32 v[6:7], v[64:65], v[90:91], v[6:7] op_sel_hi:[1,0,1]
	v_pk_fma_f32 v[4:5], v[62:63], v[90:91], v[4:5] op_sel_hi:[1,0,1]
	v_pk_fma_f32 v[10:11], v[64:65], v[98:99], v[10:11] op_sel_hi:[1,0,1]
	v_pk_fma_f32 v[8:9], v[62:63], v[98:99], v[8:9] op_sel_hi:[1,0,1]
	s_waitcnt vmcnt(25)
	v_pk_fma_f32 v[6:7], v[68:69], v[78:79], v[6:7] op_sel_hi:[1,0,1]
	v_pk_fma_f32 v[4:5], v[66:67], v[78:79], v[4:5] op_sel_hi:[1,0,1]
	v_pk_fma_f32 v[10:11], v[68:69], v[86:87], v[10:11] op_sel_hi:[1,0,1]
	v_pk_fma_f32 v[8:9], v[66:67], v[86:87], v[8:9] op_sel_hi:[1,0,1]
	s_waitcnt vmcnt(24)
	v_pk_fma_f32 v[6:7], v[72:73], v[92:93], v[6:7] op_sel_hi:[1,0,1]
	v_pk_fma_f32 v[4:5], v[70:71], v[92:93], v[4:5] op_sel_hi:[1,0,1]
	v_pk_fma_f32 v[10:11], v[72:73], v[100:101], v[10:11] op_sel_hi:[1,0,1]
	v_pk_fma_f32 v[8:9], v[70:71], v[100:101], v[8:9] op_sel_hi:[1,0,1]
	v_mov_b32_e32 v2, s8
	ds_read2_b32 v[28:29], v2 offset1:8
	v_add_u32_e32 v27, 0x2000, v2
	ds_read2_b32 v[74:75], v2 offset0:16 offset1:24
	ds_read2_b32 v[76:77], v2 offset0:32 offset1:40
	ds_read2_b32 v[78:79], v2 offset0:48 offset1:56
	ds_read2_b32 v[80:81], v27 offset1:8
	ds_read2_b32 v[82:83], v27 offset0:16 offset1:24
	ds_read2_b32 v[84:85], v27 offset0:32 offset1:40
	ds_read2_b32 v[86:87], v27 offset0:48 offset1:56
	s_waitcnt lgkmcnt(7)
	v_mov_b32_e32 v2, v29
	s_waitcnt lgkmcnt(3)
	v_mov_b32_e32 v94, v81
	v_mov_b32_e32 v88, v75
	s_waitcnt lgkmcnt(2)
	v_mov_b32_e32 v96, v83
	v_mov_b32_e32 v90, v77
	s_waitcnt lgkmcnt(1)
	v_mov_b32_e32 v98, v85
	s_addk_i32 s8, 0x100
	v_mov_b32_e32 v92, v79
	s_waitcnt lgkmcnt(0)
	v_mov_b32_e32 v100, v87
	s_waitcnt vmcnt(23)
	v_pk_fma_f32 v[6:7], v[106:107], v[28:29], v[6:7] op_sel_hi:[1,0,1]
	v_pk_fma_f32 v[4:5], v[104:105], v[28:29], v[4:5] op_sel_hi:[1,0,1]
	v_pk_fma_f32 v[10:11], v[106:107], v[80:81], v[10:11] op_sel_hi:[1,0,1]
	v_pk_fma_f32 v[8:9], v[104:105], v[80:81], v[8:9] op_sel_hi:[1,0,1]
	s_waitcnt vmcnt(22)
	v_pk_fma_f32 v[6:7], v[110:111], v[2:3], v[6:7] op_sel_hi:[1,0,1]
	v_pk_fma_f32 v[4:5], v[108:109], v[2:3], v[4:5] op_sel_hi:[1,0,1]
	v_pk_fma_f32 v[10:11], v[110:111], v[94:95], v[10:11] op_sel_hi:[1,0,1]
	v_pk_fma_f32 v[8:9], v[108:109], v[94:95], v[8:9] op_sel_hi:[1,0,1]
	s_waitcnt vmcnt(21)
	v_pk_fma_f32 v[6:7], v[114:115], v[74:75], v[6:7] op_sel_hi:[1,0,1]
	v_pk_fma_f32 v[4:5], v[112:113], v[74:75], v[4:5] op_sel_hi:[1,0,1]
	v_pk_fma_f32 v[10:11], v[114:115], v[82:83], v[10:11] op_sel_hi:[1,0,1]
	v_pk_fma_f32 v[8:9], v[112:113], v[82:83], v[8:9] op_sel_hi:[1,0,1]
	s_waitcnt vmcnt(20)
	v_pk_fma_f32 v[6:7], v[118:119], v[88:89], v[6:7] op_sel_hi:[1,0,1]
	v_pk_fma_f32 v[4:5], v[116:117], v[88:89], v[4:5] op_sel_hi:[1,0,1]
	v_pk_fma_f32 v[10:11], v[118:119], v[96:97], v[10:11] op_sel_hi:[1,0,1]
	v_pk_fma_f32 v[8:9], v[116:117], v[96:97], v[8:9] op_sel_hi:[1,0,1]
	s_waitcnt vmcnt(19)
	v_pk_fma_f32 v[6:7], v[122:123], v[76:77], v[6:7] op_sel_hi:[1,0,1]
	v_pk_fma_f32 v[4:5], v[120:121], v[76:77], v[4:5] op_sel_hi:[1,0,1]
	v_pk_fma_f32 v[10:11], v[122:123], v[84:85], v[10:11] op_sel_hi:[1,0,1]
	v_pk_fma_f32 v[8:9], v[120:121], v[84:85], v[8:9] op_sel_hi:[1,0,1]
	s_waitcnt vmcnt(18)
	v_pk_fma_f32 v[6:7], v[126:127], v[90:91], v[6:7] op_sel_hi:[1,0,1]
	v_pk_fma_f32 v[4:5], v[124:125], v[90:91], v[4:5] op_sel_hi:[1,0,1]
	v_pk_fma_f32 v[10:11], v[126:127], v[98:99], v[10:11] op_sel_hi:[1,0,1]
	v_pk_fma_f32 v[8:9], v[124:125], v[98:99], v[8:9] op_sel_hi:[1,0,1]
	s_waitcnt vmcnt(17)
	v_pk_fma_f32 v[6:7], v[130:131], v[78:79], v[6:7] op_sel_hi:[1,0,1]
	v_pk_fma_f32 v[4:5], v[128:129], v[78:79], v[4:5] op_sel_hi:[1,0,1]
	v_pk_fma_f32 v[10:11], v[130:131], v[86:87], v[10:11] op_sel_hi:[1,0,1]
	v_pk_fma_f32 v[8:9], v[128:129], v[86:87], v[8:9] op_sel_hi:[1,0,1]
	s_waitcnt vmcnt(16)
; __global__ void __launch_bounds__(NWAVES * 64, 2) fwd_kernel(Args a_unused) {
;     ...
; #pragma unroll 8
;             for (int k = k0 + wave; k < k0 + 512; k += 8) { const f32x4 wv = __builtin_nontemporal_load((const f32x4*)(A->w_mod + (size_t)k * 12288 + col)); al += sc[k] * wv; ac += scc[k] * wv; }
	v_pk_fma_f32 v[6:7], v[134:135], v[92:93], v[6:7] op_sel_hi:[1,0,1]
	v_pk_fma_f32 v[4:5], v[132:133], v[92:93], v[4:5] op_sel_hi:[1,0,1]
	v_pk_fma_f32 v[10:11], v[134:135], v[100:101], v[10:11] op_sel_hi:[1,0,1]
	v_pk_fma_f32 v[8:9], v[132:133], v[100:101], v[8:9] op_sel_hi:[1,0,1]
	v_mov_b32_e32 v2, s8
	ds_read2_b32 v[28:29], v2 offset1:8
	v_add_u32_e32 v27, 0x2000, v2
	ds_read2_b32 v[74:75], v2 offset0:16 offset1:24
	ds_read2_b32 v[76:77], v2 offset0:32 offset1:40
	ds_read2_b32 v[78:79], v2 offset0:48 offset1:56
	ds_read2_b32 v[80:81], v27 offset1:8
	ds_read2_b32 v[82:83], v27 offset0:16 offset1:24
	ds_read2_b32 v[84:85], v27 offset0:32 offset1:40
	ds_read2_b32 v[86:87], v27 offset0:48 offset1:56
	s_waitcnt lgkmcnt(7)
	v_mov_b32_e32 v2, v29
	s_waitcnt lgkmcnt(3)
	v_mov_b32_e32 v94, v81
	v_mov_b32_e32 v88, v75
	s_waitcnt lgkmcnt(2)
	v_mov_b32_e32 v96, v83
	v_mov_b32_e32 v90, v77
	s_waitcnt lgkmcnt(1)
	v_mov_b32_e32 v98, v85
	s_addk_i32 s8, 0x100
	v_mov_b32_e32 v92, v79
	s_waitcnt lgkmcnt(0)
	v_mov_b32_e32 v100, v87
	s_waitcnt vmcnt(15)
	v_pk_fma_f32 v[6:7], v[170:171], v[28:29], v[6:7] op_sel_hi:[1,0,1]
	v_pk_fma_f32 v[4:5], v[168:169], v[28:29], v[4:5] op_sel_hi:[1,0,1]
	v_pk_fma_f32 v[10:11], v[170:171], v[80:81], v[10:11] op_sel_hi:[1,0,1]
	v_pk_fma_f32 v[8:9], v[168:169], v[80:81], v[8:9] op_sel_hi:[1,0,1]
	s_waitcnt vmcnt(14)
	v_pk_fma_f32 v[6:7], v[174:175], v[2:3], v[6:7] op_sel_hi:[1,0,1]
	v_pk_fma_f32 v[4:5], v[172:173], v[2:3], v[4:5] op_sel_hi:[1,0,1]
	v_pk_fma_f32 v[10:11], v[174:175], v[94:95], v[10:11] op_sel_hi:[1,0,1]
	v_pk_fma_f32 v[8:9], v[172:173], v[94:95], v[8:9] op_sel_hi:[1,0,1]
	s_waitcnt vmcnt(13)
	v_pk_fma_f32 v[6:7], v[178:179], v[74:75], v[6:7] op_sel_hi:[1,0,1]
	v_pk_fma_f32 v[4:5], v[176:177], v[74:75], v[4:5] op_sel_hi:[1,0,1]
	v_pk_fma_f32 v[10:11], v[178:179], v[82:83], v[10:11] op_sel_hi:[1,0,1]
	v_pk_fma_f32 v[8:9], v[176:177], v[82:83], v[8:9] op_sel_hi:[1,0,1]
	s_waitcnt vmcnt(12)
	v_pk_fma_f32 v[6:7], v[182:183], v[88:89], v[6:7] op_sel_hi:[1,0,1]
	v_pk_fma_f32 v[4:5], v[180:181], v[88:89], v[4:5] op_sel_hi:[1,0,1]
	v_pk_fma_f32 v[10:11], v[182:183], v[96:97], v[10:11] op_sel_hi:[1,0,1]
	v_pk_fma_f32 v[8:9], v[180:181], v[96:97], v[8:9] op_sel_hi:[1,0,1]
	s_waitcnt vmcnt(11)
	v_pk_fma_f32 v[6:7], v[186:187], v[76:77], v[6:7] op_sel_hi:[1,0,1]
	v_pk_fma_f32 v[4:5], v[184:185], v[76:77], v[4:5] op_sel_hi:[1,0,1]
	v_pk_fma_f32 v[10:11], v[186:187], v[84:85], v[10:11] op_sel_hi:[1,0,1]
	v_pk_fma_f32 v[8:9], v[184:185], v[84:85], v[8:9] op_sel_hi:[1,0,1]
	s_waitcnt vmcnt(10)
	v_pk_fma_f32 v[6:7], v[190:191], v[90:91], v[6:7] op_sel_hi:[1,0,1]
	v_pk_fma_f32 v[4:5], v[188:189], v[90:91], v[4:5] op_sel_hi:[1,0,1]
	v_pk_fma_f32 v[10:11], v[190:191], v[98:99], v[10:11] op_sel_hi:[1,0,1]
	v_pk_fma_f32 v[8:9], v[188:189], v[98:99], v[8:9] op_sel_hi:[1,0,1]
	s_waitcnt vmcnt(9)
	v_pk_fma_f32 v[6:7], v[194:195], v[78:79], v[6:7] op_sel_hi:[1,0,1]
	v_pk_fma_f32 v[4:5], v[192:193], v[78:79], v[4:5] op_sel_hi:[1,0,1]
	v_pk_fma_f32 v[10:11], v[194:195], v[86:87], v[10:11] op_sel_hi:[1,0,1]
	v_pk_fma_f32 v[8:9], v[192:193], v[86:87], v[8:9] op_sel_hi:[1,0,1]
	s_waitcnt vmcnt(8)
	v_pk_fma_f32 v[6:7], v[198:199], v[92:93], v[6:7] op_sel_hi:[1,0,1]
	v_pk_fma_f32 v[4:5], v[196:197], v[92:93], v[4:5] op_sel_hi:[1,0,1]
	v_pk_fma_f32 v[10:11], v[198:199], v[100:101], v[10:11] op_sel_hi:[1,0,1]
	v_pk_fma_f32 v[8:9], v[196:197], v[100:101], v[8:9] op_sel_hi:[1,0,1]
	v_mov_b32_e32 v2, s8
	ds_read2_b32 v[28:29], v2 offset1:8
	v_add_u32_e32 v27, 0x2000, v2
	ds_read2_b32 v[74:75], v2 offset0:16 offset1:24
	ds_read2_b32 v[76:77], v2 offset0:32 offset1:40
	ds_read2_b32 v[78:79], v2 offset0:48 offset1:56
	ds_read2_b32 v[80:81], v27 offset1:8
	ds_read2_b32 v[82:83], v27 offset0:16 offset1:24
	ds_read2_b32 v[84:85], v27 offset0:32 offset1:40
	ds_read2_b32 v[86:87], v27 offset0:48 offset1:56
	s_waitcnt lgkmcnt(7)
	v_mov_b32_e32 v2, v29
	s_waitcnt lgkmcnt(3)
	v_mov_b32_e32 v94, v81
	v_mov_b32_e32 v88, v75
	s_waitcnt lgkmcnt(2)
	v_mov_b32_e32 v96, v83
	v_mov_b32_e32 v90, v77
	s_waitcnt lgkmcnt(1)
	v_mov_b32_e32 v98, v85
	s_addk_i32 s8, 0x100
	v_mov_b32_e32 v92, v79
	s_waitcnt lgkmcnt(0)
	v_mov_b32_e32 v100, v87
	s_waitcnt vmcnt(7)
	v_pk_fma_f32 v[6:7], v[202:203], v[28:29], v[6:7] op_sel_hi:[1,0,1]
	v_pk_fma_f32 v[4:5], v[200:201], v[28:29], v[4:5] op_sel_hi:[1,0,1]
	v_pk_fma_f32 v[10:11], v[202:203], v[80:81], v[10:11] op_sel_hi:[1,0,1]
	v_pk_fma_f32 v[8:9], v[200:201], v[80:81], v[8:9] op_sel_hi:[1,0,1]
	s_waitcnt vmcnt(6)
	v_pk_fma_f32 v[6:7], v[206:207], v[2:3], v[6:7] op_sel_hi:[1,0,1]
	v_pk_fma_f32 v[4:5], v[204:205], v[2:3], v[4:5] op_sel_hi:[1,0,1]
	v_pk_fma_f32 v[10:11], v[206:207], v[94:95], v[10:11] op_sel_hi:[1,0,1]
	v_pk_fma_f32 v[8:9], v[204:205], v[94:95], v[8:9] op_sel_hi:[1,0,1]
	s_waitcnt vmcnt(5)
	v_pk_fma_f32 v[6:7], v[210:211], v[74:75], v[6:7] op_sel_hi:[1,0,1]
	v_pk_fma_f32 v[4:5], v[208:209], v[74:75], v[4:5] op_sel_hi:[1,0,1]
	v_pk_fma_f32 v[10:11], v[210:211], v[82:83], v[10:11] op_sel_hi:[1,0,1]
	v_pk_fma_f32 v[8:9], v[208:209], v[82:83], v[8:9] op_sel_hi:[1,0,1]
	s_waitcnt vmcnt(4)
	v_pk_fma_f32 v[6:7], v[214:215], v[88:89], v[6:7] op_sel_hi:[1,0,1]
	v_pk_fma_f32 v[4:5], v[212:213], v[88:89], v[4:5] op_sel_hi:[1,0,1]
	v_pk_fma_f32 v[10:11], v[214:215], v[96:97], v[10:11] op_sel_hi:[1,0,1]
	v_pk_fma_f32 v[8:9], v[212:213], v[96:97], v[8:9] op_sel_hi:[1,0,1]
	s_waitcnt vmcnt(3)
	v_pk_fma_f32 v[6:7], v[218:219], v[76:77], v[6:7] op_sel_hi:[1,0,1]
	v_pk_fma_f32 v[4:5], v[216:217], v[76:77], v[4:5] op_sel_hi:[1,0,1]
	v_pk_fma_f32 v[10:11], v[218:219], v[84:85], v[10:11] op_sel_hi:[1,0,1]
	v_pk_fma_f32 v[8:9], v[216:217], v[84:85], v[8:9] op_sel_hi:[1,0,1]
	s_waitcnt vmcnt(2)
	v_pk_fma_f32 v[6:7], v[222:223], v[90:91], v[6:7] op_sel_hi:[1,0,1]
	v_pk_fma_f32 v[4:5], v[220:221], v[90:91], v[4:5] op_sel_hi:[1,0,1]
	v_pk_fma_f32 v[10:11], v[222:223], v[98:99], v[10:11] op_sel_hi:[1,0,1]
	v_pk_fma_f32 v[8:9], v[220:221], v[98:99], v[8:9] op_sel_hi:[1,0,1]
	s_waitcnt vmcnt(1)
	v_pk_fma_f32 v[6:7], v[226:227], v[78:79], v[6:7] op_sel_hi:[1,0,1]
	v_pk_fma_f32 v[4:5], v[224:225], v[78:79], v[4:5] op_sel_hi:[1,0,1]
	v_pk_fma_f32 v[10:11], v[226:227], v[86:87], v[10:11] op_sel_hi:[1,0,1]
	v_pk_fma_f32 v[8:9], v[224:225], v[86:87], v[8:9] op_sel_hi:[1,0,1]
	s_waitcnt vmcnt(0)
	v_pk_fma_f32 v[6:7], v[230:231], v[92:93], v[6:7] op_sel_hi:[1,0,1]
	v_pk_fma_f32 v[4:5], v[228:229], v[92:93], v[4:5] op_sel_hi:[1,0,1]
	v_pk_fma_f32 v[10:11], v[230:231], v[100:101], v[10:11] op_sel_hi:[1,0,1]
	v_pk_fma_f32 v[8:9], v[228:229], v[100:101], v[8:9] op_sel_hi:[1,0,1]

; #define LAS __attribute__((address_space(3)))
; DI int crow(int i, int h) { return (i & 3) + 8 * (i >> 2) + 4 * h; }
; #define MFMA32(a, b, c) __builtin_amdgcn_mfma_f32_32x32x16_bf16((a), (b), (c), 0, 0, 0)
; template <bool OUT>
; DI void scan_segment(LAS unsigned char* ldsb, const bf16* proj, int hh, int segF, int segB, float* Lbuf, float* Dlog, bf16* oscr) {
;     ...
;         for (int dt = 0; dt < 4; ++dt)
; #pragma unroll
;             for (int g4 = 0; g4 < 4; ++g4) { const f32x4 f = *(const LAS f32x4*)(FAC + 32 * dt + 8 * g4 + 4 * h5);
; #pragma unroll
;                 for (int j = 0; j < 4; ++j) acc[dt][4 * g4 + j] *= f[j]; }
;         if (OUT) {
;             bf16x8 qf[8];
;             f32x16 pT, oT;
; #pragma unroll
;             for (int i = 0; i < 16; ++i) { pT[i] = 0.f; oT[i] = 0.f; }
; #pragma unroll
;             for (int kk = 0; kk < 8; ++kk) {
;                 qf[kk] = lds_frag2(QH + r * RSQ + (16 * kk + 4 * h5) * 2, QH + r * RSQ + (16 * kk + 8 + 4 * h5) * 2);
;                 const bf16x8 kf = lds_frag2(KH + r * RSQ + (16 * kk + 4 * h5) * 2, KH + r * RSQ + (16 * kk + 8 + 4 * h5) * 2);
;                 pT = MFMA32(kf, qf[kk], pT);
;             }
; #pragma unroll
;             for (int i = 0; i < 16; ++i) if (crow(i, h5) > r) pT[i] = 0.f;
; #pragma unroll
;             for (int dt = 0; dt < 4; ++dt)
; #pragma unroll
;                 for (int ks = 0; ks < 2; ++ks) {
;                     const bf16x8 sa = pack8(acc[dt][8 * ks], acc[dt][8 * ks + 1], acc[dt][8 * ks + 2], acc[dt][8 * ks + 3], acc[dt][8 * ks + 4], acc[dt][8 * ks + 5], acc[dt][8 * ks + 6], acc[dt][8 * ks + 7]);
;                     oT = MFMA32(sa, qf[2 * dt + ks], oT);
;                 }
; #pragma unroll
;             for (int ks = 0; ks < 2; ++ks) {
;                 const bf16x8 pf = pack8(pT[8 * ks], pT[8 * ks + 1], pT[8 * ks + 2], pT[8 * ks + 3], pT[8 * ks + 4], pT[8 * ks + 5], pT[8 * ks + 6], pT[8 * ks + 7]);
;                 const bf16x8 va = lds_frag2(VT + (e0 + r) * RST + (16 * ks + 4 * h5) * 2, VT + (e0 + r) * RST + (16 * ks + 8 + 4 * h5) * 2);
;                 oT = MFMA32(va, pf, oT);
.LBB0_1384:
	v_add_u32_e32 v134, 0x2000, v180
	ds_read2_b64 v[66:69], v134 offset0:32 offset1:34
	ds_read2_b64 v[98:101], v180 offset1:2
	ds_read2_b64 v[206:209], v134 offset0:36 offset1:38
	ds_read2_b64 v[102:105], v180 offset0:4 offset1:6
	ds_read2_b64 v[210:213], v134 offset0:40 offset1:42
	ds_read2_b64 v[106:109], v180 offset0:8 offset1:10
	ds_read2_b64 v[214:217], v134 offset0:44 offset1:46
	ds_read2_b64 v[110:113], v180 offset0:12 offset1:14
	ds_read2_b64 v[218:221], v134 offset0:48 offset1:50
	ds_read2_b64 v[114:117], v180 offset0:16 offset1:18
	ds_read2_b64 v[70:73], v134 offset0:52 offset1:54
	ds_read2_b64 v[118:121], v180 offset0:20 offset1:22
	ds_read2_b64 v[130:133], v134 offset0:56 offset1:58
	ds_read2_b64 v[122:125], v180 offset0:24 offset1:26
	ds_read2_b64 v[134:137], v134 offset0:60 offset1:62
	s_waitcnt lgkmcnt(13)
	v_mfma_f32_32x32x16_bf16 v[82:97], v[66:69], v[98:101], 0
	ds_read2_b64 v[146:149], v180 offset0:28 offset1:30
	ds_read_b128 v[66:69], v176 offset:35328
	s_waitcnt lgkmcnt(13)
	v_mfma_f32_32x32x16_bf16 v[82:97], v[206:209], v[102:105], v[82:97]
	ds_read_b128 v[74:77], v176 offset:35360
	ds_read_b128 v[78:81], v176 offset:35392
	s_waitcnt lgkmcnt(13)
	v_mfma_f32_32x32x16_bf16 v[82:97], v[210:213], v[106:109], v[82:97]
	ds_read_b128 v[126:129], v176 offset:35424
	ds_read_b128 v[222:225], v176 offset:35456
	s_waitcnt lgkmcnt(13)
	v_mfma_f32_32x32x16_bf16 v[82:97], v[214:217], v[110:113], v[82:97]
	ds_read_b128 v[226:229], v176 offset:35488
	ds_read_b128 v[230:233], v176 offset:35520
	s_waitcnt lgkmcnt(13)
	v_mfma_f32_32x32x16_bf16 v[82:97], v[218:221], v[114:117], v[82:97]
	ds_read_b128 v[234:237], v176 offset:35552
	ds_read_b128 v[238:241], v176 offset:35584
	s_waitcnt lgkmcnt(8)
	v_pk_mul_f32 v[66:67], v[2:3], v[66:67]
	v_pk_mul_f32 v[68:69], v[4:5], v[68:69]
	v_mfma_f32_32x32x16_bf16 v[82:97], v[70:73], v[118:121], v[82:97]
	s_waitcnt lgkmcnt(7)
	v_mul_f32_e64 v70, v6, v74
	v_mul_f32_e64 v71, v7, v75
	v_mul_f32_e64 v72, v8, v76
	v_mul_f32_e64 v73, v9, v77
	s_waitcnt lgkmcnt(6)
	v_mul_f32_e64 v74, v10, v78
	v_mul_f32_e64 v75, v11, v79
	v_pk_mul_f32 v[76:77], v[12:13], v[80:81]
	s_waitcnt lgkmcnt(5)
	v_pk_mul_f32 v[78:79], v[14:15], v[126:127]
	v_pk_mul_f32 v[80:81], v[16:17], v[128:129]
	ds_read_b128 v[242:245], v176 offset:35616
	ds_read_b128 v[246:249], v176 offset:35648
	ds_read_b128 v[250:253], v176 offset:35680
	ds_read_b128 v[206:209], v176 offset:35712
	ds_read_b128 v[210:213], v176 offset:35744
	v_cvt_pk_bf16_f32 v126, v66, v67
	v_mfma_f32_32x32x16_bf16 v[82:97], v[130:133], v[122:125], v[82:97]
	v_cvt_pk_bf16_f32 v127, v68, v69
	v_cvt_pk_bf16_f32 v128, v70, v71
	v_cvt_pk_bf16_f32 v129, v72, v73
	v_cvt_pk_bf16_f32 v186, v74, v75
	v_cvt_pk_bf16_f32 v187, v76, v77
	v_cvt_pk_bf16_f32 v188, v78, v79
	v_cvt_pk_bf16_f32 v189, v80, v81
	ds_read_b128 v[214:217], v176 offset:35776
	ds_read_b128 v[218:221], v176 offset:35808
	v_mfma_f32_32x32x16_bf16 v[82:97], v[134:137], v[146:149], v[82:97]
	s_nop 11
	v_cndmask_b32_e64 v130, v82, 0, s[4:5]
	v_cndmask_b32_e64 v204, v130, v82, s[6:7]
	v_mfma_f32_32x32x16_bf16 v[130:145], v[126:129], v[98:101], 0
	v_cndmask_b32_e64 v185, 0, v83, s[6:7]
	v_cndmask_b32_e64 v190, v84, 0, s[8:9]
	v_cndmask_b32_e64 v191, v85, 0, s[10:11]
	v_cndmask_b32_e64 v192, v86, 0, s[12:13]
	v_cndmask_b32_e64 v193, v87, 0, s[14:15]
	v_cndmask_b32_e64 v194, v88, 0, s[16:17]
	v_cndmask_b32_e64 v195, v89, 0, s[18:19]
	v_mfma_f32_32x32x16_bf16 v[130:145], v[186:189], v[102:105], v[130:145]
	v_cndmask_b32_e64 v196, v90, 0, s[20:21]
	v_cndmask_b32_e64 v197, v91, 0, s[22:23]
	s_waitcnt lgkmcnt(11)
	v_mul_f32_e64 v82, v18, v222
	v_mul_f32_e64 v83, v19, v223
	v_pk_mul_f32 v[84:85], v[20:21], v[224:225]
	s_waitcnt lgkmcnt(10)
	v_pk_mul_f32 v[86:87], v[22:23], v[226:227]
	v_pk_mul_f32 v[88:89], v[24:25], v[228:229]
	v_add_u32_e32 v186, v177, v169
	v_add_u32_e32 v186, 0x6000, v186
	ds_read2_b64 v[222:225], v186 offset0:192 offset1:194
	ds_read2_b64 v[226:229], v186 offset0:196 offset1:198
	v_cndmask_b32_e64 v198, v92, 0, s[24:25]
	v_cndmask_b32_e64 v199, v93, 0, s[26:27]
	v_cvt_pk_bf16_f32 v90, v82, v83
	v_cvt_pk_bf16_f32 v91, v84, v85
	v_cvt_pk_bf16_f32 v92, v86, v87
	v_cvt_pk_bf16_f32 v93, v88, v89
	v_cndmask_b32_e64 v200, v94, 0, s[28:29]
	v_cndmask_b32_e64 v201, v95, 0, s[30:31]
	v_cndmask_b32_e64 v202, v96, 0, s[34:35]
	v_cndmask_b32_e64 v203, v97, 0, s[36:37]
	v_mfma_f32_32x32x16_bf16 v[130:145], v[90:93], v[106:109], v[130:145]
	s_waitcnt lgkmcnt(11)
	v_mul_f32_e64 v90, v26, v230
	v_mul_f32_e64 v91, v27, v231
	v_pk_mul_f32 v[92:93], v[28:29], v[232:233]
	s_waitcnt lgkmcnt(10)
; DI unsigned pk2(float lo, float hi) { f32x2 v = {lo, hi}; bf16x2_t b = __builtin_convertvector(v, bf16x2_t); return __builtin_bit_cast(unsigned, b); }
; #define MFMA32(a, b, c) __builtin_amdgcn_mfma_f32_32x32x16_bf16((a), (b), (c), 0, 0, 0)
; template <bool OUT>
; DI void scan_segment(LAS unsigned char* ldsb, const bf16* proj, int hh, int segF, int segB, float* Lbuf, float* Dlog, bf16* oscr) {
;     ...
;             for (int dt = 0; dt < 4; ++dt)
; #pragma unroll
;                 for (int ks = 0; ks < 2; ++ks) {
;                     const bf16x8 sa = pack8(acc[dt][8 * ks], acc[dt][8 * ks + 1], acc[dt][8 * ks + 2], acc[dt][8 * ks + 3], acc[dt][8 * ks + 4], acc[dt][8 * ks + 5], acc[dt][8 * ks + 6], acc[dt][8 * ks + 7]);
;                     oT = MFMA32(sa, qf[2 * dt + ks], oT);
;                 }
; #pragma unroll
;             for (int ks = 0; ks < 2; ++ks) {
;                 const bf16x8 pf = pack8(pT[8 * ks], pT[8 * ks + 1], pT[8 * ks + 2], pT[8 * ks + 3], pT[8 * ks + 4], pT[8 * ks + 5], pT[8 * ks + 6], pT[8 * ks + 7]);
;                 const bf16x8 va = lds_frag2(VT + (e0 + r) * RST + (16 * ks + 4 * h5) * 2, VT + (e0 + r) * RST + (16 * ks + 8 + 4 * h5) * 2);
;                 oT = MFMA32(va, pf, oT);
;             }
;             bf16* orow = oscr + ((size_t)(dir * 8 + hh) * NTOK + (rb + sgn * r)) * 128 + e0 + 4 * h5;
; #pragma unroll
;             for (int g4 = 0; g4 < 4; ++g4) { u32x2 o; o.x = pk2(oT[4 * g4], oT[4 * g4 + 1]); o.y = pk2(oT[4 * g4 + 2], oT[4 * g4 + 3]); *(u32x2*)(orow + 8 * g4) = o; }
;         }
; #pragma unroll
;         for (int ks = 0; ks < 2; ++ks) {
;             const bf16x8 vb = lds_frag2(VT + (e0 + r) * RST + (16 * ks + 8 * h5) * 2, VT + (e0 + r) * RST + (16 * ks + 8 * h5) * 2 + 8);
; #pragma unroll
;             for (int dt = 0; dt < 4; ++dt) {
;                 const bf16x8 ka = lds_frag2(KT + (32 * dt + r) * RST + (16 * ks + 8 * h5) * 2, KT + (32 * dt + r) * RST + (16 * ks + 8 * h5) * 2 + 8);
;                 acc[dt] = MFMA32(ka, vb, acc[dt]);
;             }
;         }
	v_pk_mul_f32 v[94:95], v[30:31], v[234:235]
	v_pk_mul_f32 v[96:97], v[32:33], v[236:237]
	v_add_u32_e32 v186, 0x5400, v181
	ds_read2_b64 v[230:233], v186 offset1:1
	v_add_u32_e32 v186, v177, v167
	v_add_u32_e32 v186, 0x6600, v186
	ds_read2_b64 v[234:237], v186 offset1:1
	v_cvt_pk_bf16_f32 v98, v90, v91
	v_cvt_pk_bf16_f32 v99, v92, v93
	v_cvt_pk_bf16_f32 v100, v94, v95
	v_cvt_pk_bf16_f32 v101, v96, v97
	s_nop 1
	v_mfma_f32_32x32x16_bf16 v[130:145], v[98:101], v[110:113], v[130:145]
	s_waitcnt lgkmcnt(11)
	v_mul_f32_e64 v98, v34, v238
	v_mul_f32_e64 v99, v35, v239
	v_pk_mul_f32 v[100:101], v[36:37], v[240:241]
	s_waitcnt lgkmcnt(10)
	v_pk_mul_f32 v[102:103], v[38:39], v[242:243]
	v_pk_mul_f32 v[104:105], v[40:41], v[244:245]
	v_add_u32_e32 v186, 0x4200, v181
	ds_read2_b64 v[238:241], v186 offset1:1
	v_add_u32_e32 v186, 0x4b00, v181
	ds_read2_b64 v[242:245], v186 offset1:1
	v_cvt_pk_bf16_f32 v106, v98, v99
	v_cvt_pk_bf16_f32 v107, v100, v101
	v_cvt_pk_bf16_f32 v108, v102, v103
	v_cvt_pk_bf16_f32 v109, v104, v105
	s_nop 1
	v_mfma_f32_32x32x16_bf16 v[130:145], v[106:109], v[114:117], v[130:145]
	s_waitcnt lgkmcnt(11)
	v_mul_f32_e64 v106, v42, v246
	v_mul_f32_e64 v107, v43, v247
	v_pk_mul_f32 v[108:109], v[44:45], v[248:249]
	s_waitcnt lgkmcnt(10)
	v_pk_mul_f32 v[110:111], v[46:47], v[250:251]
	v_pk_mul_f32 v[112:113], v[48:49], v[252:253]
	v_add_u32_e32 v186, 0x5d00, v181
	ds_read2_b64 v[246:249], v186 offset1:1
	v_add_u32_e32 v186, v177, v167
	v_add_u32_e32 v186, 0x6620, v186
	ds_read2_b64 v[250:253], v186 offset1:1
	v_cvt_pk_bf16_f32 v114, v106, v107
	v_cvt_pk_bf16_f32 v115, v108, v109
	v_cvt_pk_bf16_f32 v116, v110, v111
	v_cvt_pk_bf16_f32 v117, v112, v113
	s_nop 1
	v_mfma_f32_32x32x16_bf16 v[130:145], v[114:117], v[118:121], v[130:145]
	s_waitcnt lgkmcnt(11)
	v_mul_f32_e64 v114, v50, v206
	v_mul_f32_e64 v115, v51, v207
	v_pk_mul_f32 v[116:117], v[52:53], v[208:209]
	s_waitcnt lgkmcnt(10)
	v_pk_mul_f32 v[118:119], v[54:55], v[210:211]
	v_pk_mul_f32 v[120:121], v[56:57], v[212:213]
	v_add_u32_e32 v186, 0x4220, v181
	ds_read2_b64 v[206:209], v186 offset1:1
	v_add_u32_e32 v186, 0x4b20, v181
	ds_read2_b64 v[210:213], v186 offset1:1
	v_cvt_pk_bf16_f32 v126, v114, v115
	v_cvt_pk_bf16_f32 v127, v116, v117
	v_cvt_pk_bf16_f32 v128, v118, v119
	v_cvt_pk_bf16_f32 v129, v120, v121
	s_nop 1
	v_mfma_f32_32x32x16_bf16 v[130:145], v[126:129], v[122:125], v[130:145]
	s_waitcnt lgkmcnt(11)
	v_mul_f32_e64 v122, v58, v214
	v_mul_f32_e64 v123, v59, v215
	v_pk_mul_f32 v[124:125], v[60:61], v[216:217]
	s_waitcnt lgkmcnt(10)
	v_pk_mul_f32 v[126:127], v[62:63], v[218:219]
	v_pk_mul_f32 v[128:129], v[64:65], v[220:221]
	v_add_u32_e32 v186, 0x5420, v181
	ds_read2_b64 v[214:217], v186 offset1:1
	v_add_u32_e32 v186, 0x5d20, v181
	ds_read2_b64 v[218:221], v186 offset1:1
	v_cvt_pk_bf16_f32 v186, v122, v123
	v_cvt_pk_bf16_f32 v187, v124, v125
	v_cvt_pk_bf16_f32 v188, v126, v127
	v_cvt_pk_bf16_f32 v189, v128, v129
	s_nop 1
	v_mfma_f32_32x32x16_bf16 v[130:145], v[186:189], v[146:149], v[130:145]
	v_cvt_pk_bf16_f32 v146, v204, v185
	v_cvt_pk_bf16_f32 v147, v190, v191
	v_cvt_pk_bf16_f32 v148, v192, v193
	v_cvt_pk_bf16_f32 v149, v194, v195
	s_waitcnt lgkmcnt(11)
	s_nop 0
	v_mfma_f32_32x32x16_bf16 v[130:145], v[222:225], v[146:149], v[130:145]
	v_cvt_pk_bf16_f32 v146, v196, v197
	v_cvt_pk_bf16_f32 v147, v198, v199
	v_cvt_pk_bf16_f32 v148, v200, v201
	v_cvt_pk_bf16_f32 v149, v202, v203
	s_waitcnt lgkmcnt(10)
	s_nop 0
	v_mfma_f32_32x32x16_bf16 v[130:145], v[226:229], v[146:149], v[130:145]
	s_waitcnt lgkmcnt(8)
	v_mfma_f32_32x32x16_bf16 v[98:113], v[230:233], v[234:237], v[98:113]
	s_waitcnt lgkmcnt(7)
	v_mfma_f32_32x32x16_bf16 v[66:81], v[238:241], v[234:237], v[66:81]
	s_waitcnt lgkmcnt(6)
	v_mfma_f32_32x32x16_bf16 v[82:97], v[242:245], v[234:237], v[82:97]
	s_waitcnt lgkmcnt(5)
	v_mfma_f32_32x32x16_bf16 v[114:129], v[246:249], v[234:237], v[114:129]
	s_nop 3
	v_cvt_pk_bf16_f32 v138, v138, v139
	v_cvt_pk_bf16_f32 v139, v140, v141
	v_cvt_pk_bf16_f32 v140, v142, v143
	v_cvt_pk_bf16_f32 v141, v144, v145
	s_waitcnt lgkmcnt(3)
	v_mfma_f32_32x32x16_bf16 v[66:81], v[206:209], v[250:253], v[66:81]
	v_cvt_pk_bf16_f32 v148, v134, v135
	v_add_u32_e32 v134, vcc_lo, v178
	v_ashrrev_i32_e32 v135, 31, v134
	v_lshlrev_b64 v[134:135], 8, v[134:135]
	v_cvt_pk_bf16_f32 v146, v130, v131
	v_lshl_add_u64 v[142:143], v[160:161], 0, v[134:135]
	v_cvt_pk_bf16_f32 v147, v132, v133
	v_cvt_pk_bf16_f32 v149, v136, v137
	s_waitcnt lgkmcnt(2)
	v_mfma_f32_32x32x16_bf16 v[82:97], v[210:213], v[250:253], v[82:97]
	s_andn2_b64 vcc, exec, s[38:39]
	global_store_dwordx2 v[142:143], v[146:147], off
	global_store_dwordx2 v[142:143], v[148:149], off offset:16
	global_store_dwordx2 v[142:143], v[138:139], off offset:32
	global_store_dwordx2 v[142:143], v[140:141], off offset:48
	s_waitcnt lgkmcnt(1)
	v_mfma_f32_32x32x16_bf16 v[98:113], v[214:217], v[250:253], v[98:113]
	s_waitcnt lgkmcnt(0)
	v_mfma_f32_32x32x16_bf16 v[114:129], v[218:221], v[250:253], v[114:129]
	s_cbranch_vccnz .LBB0_1386
	s_waitcnt vmcnt(4)
